# speedup vs baseline: 1.0442x; 1.0040x over previous
_Z6k_mainPKfPKDv8_DF16_S0_S3_S0_S0_S0_S0_S0_S0_S0_S0_S0_S3_S0_S0_S0_S0_S0_S0_S0_S0_S0_S0_S0_S0_S0_Pf:
	s_load_dwordx4 s[60:63], s[0:1], 0xd0
	s_load_dwordx8 s[12:19], s[0:1], 0xb0
	s_load_dwordx8 s[36:43], s[0:1], 0x90
	s_load_dwordx8 s[44:51], s[0:1], 0x70
	s_load_dwordx2 s[10:11], s[0:1], 0x60
	s_load_dwordx8 s[24:31], s[0:1], 0x40
	s_load_dwordx2 s[20:21], s[0:1], 0x0
	s_load_dwordx8 s[52:59], s[0:1], 0x20
	s_load_dwordx4 s[84:87], s[0:1], 0x8
	s_movk_i32 s6, 0xe0
	v_mov_b32_e32 v1, 0xffffff1f
	v_cmp_lt_u32_e64 s[6:7], s6, v0
	s_movk_i32 s4, 0xe1
	s_movk_i32 s8, 0x1c2
	v_cndmask_b32_e64 v1, 0, v1, s[6:7]
	v_readfirstlane_b32 s3, v0
	v_cmp_gt_u32_e64 s[4:5], s4, v0
	v_add_u32_e32 v8, v1, v0
	v_cmp_gt_u32_e64 s[8:9], s8, v0
	s_and_b32 s88, s2, 7
	s_mul_i32 s88, s88, 0x30000
	s_waitcnt lgkmcnt(0)
	s_add_u32 s84, s84, s88
	s_addc_u32 s85, s85, 0
	s_add_u32 s86, s86, s88
	s_addc_u32 s87, s87, 0
	v_and_b32_e32 v30, 63, v0
	v_lshlrev_b32_e32 v30, 4, v30
	v_mov_b32_e32 v31, 0
	v_lshl_add_u64 v[32:33], s[84:85], 0, v[30:31]
	v_add_co_u32_e32 v32, vcc, 0x1000, v32
	v_bfe_u32 v34, v0, 5, 1
	v_lshlrev_b32_e32 v34, 2, v34
	v_addc_co_u32_e32 v33, vcc, 0, v33, vcc
	global_load_dwordx4 v[86:89], v30, s[84:85]
	global_load_dwordx4 v[62:65], v30, s[84:85] offset:1024
	global_load_dwordx4 v[58:61], v30, s[84:85] offset:2048
	global_load_dwordx4 v[54:57], v30, s[84:85] offset:3072
	global_load_dwordx4 v[50:53], v[32:33], off
	global_load_dword v46, v34, s[86:87]
	global_load_dword v47, v34, s[86:87] offset:8
	global_load_dword v48, v34, s[86:87] offset:16
	global_load_dword v49, v34, s[86:87] offset:24
	s_and_saveexec_b64 s[22:23], s[8:9]
	s_cbranch_execz .LBB1_4
	s_mul_i32 s34, s2, 0x6978
	s_mul_hi_i32 s33, s2, 0x6978
	s_waitcnt lgkmcnt(0)
	s_add_u32 s34, s20, s34
	v_mov_b32_e32 v1, 0x3840
	s_addc_u32 s35, s21, s33
	v_cndmask_b32_e64 v2, 0, v1, s[6:7]
	v_mov_b32_e32 v3, 0
	v_lshl_add_u64 v[4:5], s[34:35], 0, v[2:3]
	v_mov_b32_e32 v9, v3
	v_lshl_add_u64 v[4:5], v[8:9], 2, v[4:5]
	s_movk_i32 s33, 0x1000
	v_add_co_u32_e32 v16, vcc, s33, v4
	v_mov_b32_e32 v7, v3
	s_nop 0
	v_addc_co_u32_e32 v17, vcc, 0, v5, vcc
	global_load_dword v1, v[4:5], off
	global_load_dword v2, v[4:5], off offset:900
	global_load_dword v6, v[4:5], off offset:1800
	global_load_dword v9, v[4:5], off offset:2700
	global_load_dword v10, v[4:5], off offset:3600
	global_load_dword v11, v[16:17], off offset:404
	global_load_dword v12, v[16:17], off offset:1304
	global_load_dword v13, v[16:17], off offset:2204
	v_add_co_u32_e32 v18, vcc, 0x2000, v4
	s_nop 1
	v_addc_co_u32_e32 v19, vcc, 0, v5, vcc
	global_load_dword v14, v[16:17], off offset:3104
	s_nop 0
	global_load_dword v16, v[16:17], off offset:4004
	s_nop 0
	global_load_dword v17, v[18:19], off offset:808
	global_load_dword v28, v[18:19], off offset:1708
	global_load_dword v27, v[18:19], off offset:2608
	global_load_dword v29, v[18:19], off offset:3508
	s_and_saveexec_b64 s[34:35], s[4:5]
	s_cbranch_execz .LBB1_3
	v_add_co_u32_e32 v4, vcc, 0x3000, v4
	s_nop 1
	v_addc_co_u32_e32 v5, vcc, 0, v5, vcc
	global_load_dword v3, v[4:5], off offset:312
	s_nop 0
	global_load_dword v4, v[4:5], off offset:1212
	s_waitcnt vmcnt(1)
	v_cvt_f16_f32_e32 v3, v3
	s_waitcnt vmcnt(0)
	v_cvt_f16_f32_e32 v7, v4

.LBB1_4:
	s_or_b64 exec, exec, s[22:23]
	s_load_dwordx4 s[68:71], s[0:1], 0x8
	s_load_dwordx2 s[4:5], s[0:1], 0x18
	s_and_b32 s22, s2, 7
	s_bfe_u32 s66, s3, 0x20006
	s_lshr_b32 s67, s3, 8
	s_mul_i32 s33, s22, 0x30000
	s_waitcnt lgkmcnt(0)
	s_add_u32 s22, s4, s33
	s_addc_u32 s23, s5, 0
	s_add_u32 s4, s68, s33
	s_addc_u32 s5, s69, 0
	s_add_u32 s34, s70, s33
	s_addc_u32 s35, s71, 0
	s_lshl_b32 s68, s66, 6
	s_mul_i32 s69, s67, 0x900
	v_and_b32_e32 v100, 63, v0
	s_or_b32 s64, s68, s69
	v_or_b32_e32 v2, s64, v100
	s_add_i32 s65, s64, 0x100
	v_ashrrev_i32_e32 v3, 31, v2
	v_or_b32_e32 v4, s65, v100
	v_lshl_add_u64 v[2:3], v[2:3], 4, s[22:23]
	v_ashrrev_i32_e32 v5, 31, v4
	s_add_i32 s65, s64, 0x200
	v_lshl_add_u64 v[4:5], v[4:5], 4, s[22:23]
	global_load_dwordx4 v[82:85], v[2:3], off
	global_load_dwordx4 v[74:77], v[4:5], off
	v_or_b32_e32 v2, s65, v100
	s_add_i32 s65, s64, 0x300
	v_ashrrev_i32_e32 v3, 31, v2
	v_or_b32_e32 v4, s65, v100
	v_lshl_add_u64 v[2:3], v[2:3], 4, s[22:23]
	v_ashrrev_i32_e32 v5, 31, v4
	s_addk_i32 s64, 0x400
	v_lshl_add_u64 v[4:5], v[4:5], 4, s[22:23]
	global_load_dwordx4 v[78:81], v[2:3], off
	global_load_dwordx4 v[70:73], v[4:5], off
	v_or_b32_e32 v2, s64, v100
	v_ashrrev_i32_e32 v3, 31, v2
	v_lshl_add_u64 v[2:3], v[2:3], 4, s[22:23]
	v_mov_b32_e32 v99, 0
	v_lshlrev_b32_e32 v98, 4, v100
	global_load_dwordx4 v[66:69], v[2:3], off
	s_add_i32 s65, s64, 0x100
	v_or_b32_e32 v2, s65, v100
	v_mov_b32_e32 v3, 0
	v_lshl_add_u64 v[2:3], v[2:3], 4, s[22:23]
	global_load_dwordx4 v[108:111], v[2:3], off
	s_add_i32 s65, s64, 0x200
	v_or_b32_e32 v2, s65, v100
	v_mov_b32_e32 v3, 0
	v_lshl_add_u64 v[2:3], v[2:3], 4, s[22:23]
	global_load_dwordx4 v[118:121], v[2:3], off
	s_add_i32 s65, s64, 0x300
	v_or_b32_e32 v2, s65, v100
	v_mov_b32_e32 v3, 0
	v_lshl_add_u64 v[2:3], v[2:3], 4, s[22:23]
	global_load_dwordx4 v[122:125], v[2:3], off
	v_bfe_u32 v115, v0, 5, 1
	s_cmp_gt_u32 s3, 63
	s_cselect_b64 s[34:35], -1, 0
	s_and_b64 vcc, exec, s[34:35]
	s_cbranch_vccz .LBB1_46
	v_cmp_gt_u32_e64 s[4:5], 21, v0
	v_lshlrev_b32_e32 v1, 2, v0
	s_and_saveexec_b64 s[64:65], s[4:5]
	s_cbranch_execnz .LBB1_47

.LBB1_15:
	s_or_b64 exec, exec, s[12:13]
	v_and_b32_e32 v114, 31, v0
	s_mul_i32 s9, s67, 0x60
	v_or_b32_e32 v15, s9, v114
	v_min_u32_e32 v91, 0xa8, v15
	v_mul_lo_u16_e32 v15, 0x4f, v91
	s_lshl_b32 s7, s66, 3
	v_lshrrev_b16_e32 v15, 9, v15
	s_or_b32 s8, s7, 0xb600
	v_and_b32_e32 v15, 62, v15
	v_add_u32_e32 v15, v91, v15
	s_movk_i32 s6, 0x48
	v_mov_b32_e32 v99, s8
	v_mad_u32_u24 v42, v15, s6, v99
	v_mad_u32_u24 v43, v115, s6, v42
	s_waitcnt lgkmcnt(0)
	s_barrier
	ds_read2_b64 v[34:37], v43 offset1:1
	ds_read2_b64 v[38:41], v43 offset0:135 offset1:136
	v_mov_b32_e32 v2, v46
	v_mov_b32_e32 v3, v46
	v_mov_b32_e32 v4, v46
	v_mov_b32_e32 v5, v46
	v_mov_b32_e32 v6, v47
	v_mov_b32_e32 v7, v47
	v_mov_b32_e32 v8, v47
	v_mov_b32_e32 v9, v47
	v_mov_b32_e32 v10, v48
	v_mov_b32_e32 v11, v48
	v_mov_b32_e32 v12, v48
	v_mov_b32_e32 v13, v48
	v_mov_b32_e32 v14, v49
	v_mov_b32_e32 v15, v49
	v_mov_b32_e32 v16, v49
	v_mov_b32_e32 v17, v49
	s_movk_i32 s8, 0x438
	s_add_i32 s12, s9, 32
	s_waitcnt lgkmcnt(1)
	v_mfma_f32_32x32x16_f16 v[18:33], v[86:89], v[34:37], v[2:17]
	v_add_u32_e32 v34, 0x8b8, v43
	ds_read2_b64 v[34:37], v34 offset1:1
	v_and_or_b32 v107, v0, 32, s7
	s_movk_i32 s7, 0x110
	v_mad_u32_u24 v91, v91, s7, v107
	s_add_i32 s9, s9, 64
	s_lshr_b32 s42, s3, 6
	s_waitcnt lgkmcnt(1)
	v_mfma_f32_32x32x16_f16 v[18:33], v[62:65], v[38:41], v[18:33]
	v_mad_u32_u24 v38, v115, s8, v42
	ds_read2_b64 v[38:41], v38 offset0:18 offset1:19
	s_cmpk_lt_u32 s3, 0x100
	s_cselect_b64 s[30:31], -1, 0
	s_add_i32 s13, s69, 0x600
	s_add_i32 s14, s69, 0x700
	v_lshlrev_b32_e32 v116, 4, v115
	s_waitcnt lgkmcnt(1)
	v_mfma_f32_32x32x16_f16 v[18:33], v[58:61], v[34:37], v[18:33]
	v_add_u32_e32 v34, 0x870, v43
	ds_read2_b64 v[34:37], v34 offset1:1
	s_movk_i32 s15, 0x1070
	s_movk_i32 s16, 0x1ba0
	s_movk_i32 s17, 0x1c20
	s_waitcnt lgkmcnt(1)
	v_mfma_f32_32x32x16_f16 v[18:33], v[54:57], v[38:41], v[18:33]
	v_or_b32_e32 v38, s12, v114
	v_min_u32_e32 v101, 0xa8, v38
	v_mul_lo_u16_e32 v38, 0x4f, v101
	v_lshrrev_b16_e32 v38, 9, v38
	v_and_b32_e32 v38, 62, v38
	v_add_u32_e32 v38, v101, v38
	v_mad_u32_u24 v97, v38, s6, v99
	v_mad_u32_u24 v106, v115, s6, v97
	ds_read2_b64 v[92:95], v106 offset1:1
	v_add_u32_e32 v96, 0x8b8, v106
	ds_read2_b64 v[102:105], v96 offset1:1
	s_waitcnt lgkmcnt(2)
	v_mfma_f32_32x32x16_f16 v[18:33], v[50:53], v[34:37], v[18:33]
	s_add_i32 s12, s69, 0x500
	s_addk_i32 s69, 0x800
	s_cmpk_gt_u32 s3, 0xff
	s_cselect_b64 vcc, -1, 0
	s_waitcnt lgkmcnt(1)
	v_mfma_f32_32x32x16_f16 v[34:49], v[86:89], v[92:95], v[2:17]
	ds_read2_b64 v[92:95], v106 offset0:135 offset1:136
	s_nop 4
	v_cvt_pk_f16_f32 v18, v18, v19
	v_pk_max_f16 v96, v18, 0
	v_mad_u32_u24 v18, v115, s8, v97
	v_cvt_pk_f16_f32 v22, v22, v23
	v_add_u32_e32 v23, 0x870, v106
	v_cvt_pk_f16_f32 v30, v30, v31
	s_waitcnt lgkmcnt(0)
	v_mfma_f32_32x32x16_f16 v[34:49], v[62:65], v[92:95], v[34:49]
	v_cvt_pk_f16_f32 v92, v20, v21
	ds_read2_b64 v[18:21], v18 offset0:18 offset1:19
	v_pk_max_f16 v97, v92, 0
	ds_read2_b64 v[92:95], v23 offset1:1
	v_cvt_pk_f16_f32 v31, v32, v33
	v_mfma_f32_32x32x16_f16 v[34:49], v[58:61], v[102:105], v[34:49]
	v_or_b32_e32 v102, 64, v114
	s_waitcnt lgkmcnt(1)
	v_mfma_f32_32x32x16_f16 v[34:49], v[54:57], v[18:21], v[34:49]
	v_cvt_pk_f16_f32 v19, v24, v25
	v_pk_max_f16 v18, v22, 0
	v_pk_max_f16 v19, v19, 0
	ds_write2_b64 v91, v[96:97], v[18:19] offset1:8
	v_cvt_pk_f16_f32 v18, v26, v27
	v_pk_max_f16 v26, v18, 0
	v_or_b32_e32 v18, s9, v114
	v_cvt_pk_f16_f32 v22, v28, v29
	v_min_u32_e32 v28, 0xa8, v18
	v_mul_lo_u16_e32 v18, 0x4f, v28
	v_lshrrev_b16_e32 v18, 9, v18
	v_and_b32_e32 v18, 62, v18
	v_add_u32_e32 v18, v28, v18
	v_mad_u32_u24 v29, v18, s6, v99
	s_waitcnt lgkmcnt(1)
	v_mfma_f32_32x32x16_f16 v[34:49], v[50:53], v[92:95], v[34:49]
	v_add_u32_e32 v94, s68, v100
	v_add_u32_e32 v94, s69, v94
	v_mov_b32_e32 v95, 0
	v_lshl_add_u64 v[94:95], v[94:95], 4, s[22:23]
	global_load_dwordx4 v[94:97], v[94:95], off
	v_mad_u32_u24 v92, v115, s6, v29
	ds_read2_b64 v[18:21], v92 offset1:1
	v_pk_max_f16 v27, v22, 0
	ds_read2_b64 v[22:25], v92 offset0:135 offset1:136
	v_or_b32_e32 v99, 32, v114
	s_nop 6
	v_cvt_pk_f16_f32 v32, v40, v41
	s_waitcnt lgkmcnt(1)
	v_mfma_f32_32x32x16_f16 v[2:17], v[86:89], v[18:21], v[2:17]
	v_pk_max_f16 v18, v30, 0
	v_pk_max_f16 v19, v31, 0
	ds_write2_b64 v91, v[26:27], v[18:19] offset0:16 offset1:24
	v_cvt_pk_f16_f32 v18, v34, v35
	v_cvt_pk_f16_f32 v19, v36, v37
	v_pk_max_f16 v26, v18, 0
	v_add_u32_e32 v18, 0x8b8, v92
	s_waitcnt lgkmcnt(1)
	v_mfma_f32_32x32x16_f16 v[2:17], v[62:65], v[22:25], v[2:17]
	v_pk_max_f16 v27, v19, 0
	ds_read2_b64 v[18:21], v18 offset1:1
	v_mad_u32_u24 v22, v115, s8, v29
	ds_read2_b64 v[22:25], v22 offset0:18 offset1:19
	v_cvt_pk_f16_f32 v31, v38, v39
	v_mad_u32_u24 v30, v101, s7, v107
	s_and_b64 s[8:9], vcc, exec
	s_waitcnt lgkmcnt(1)
	v_mfma_f32_32x32x16_f16 v[2:17], v[58:61], v[18:21], v[2:17]
	v_pk_max_f16 v18, v31, 0
	v_pk_max_f16 v19, v32, 0
	ds_write2_b64 v30, v[26:27], v[18:19] offset1:8
	v_cvt_pk_f16_f32 v18, v42, v43
	v_cvt_pk_f16_f32 v19, v44, v45
	v_pk_max_f16 v26, v18, 0
	v_add_u32_e32 v18, 0x870, v92
	s_waitcnt lgkmcnt(1)
	v_mfma_f32_32x32x16_f16 v[2:17], v[54:57], v[22:25], v[2:17]
	v_pk_max_f16 v27, v19, 0
	ds_read2_b64 v[18:21], v18 offset1:1
	v_cvt_pk_f16_f32 v22, v46, v47
	v_cvt_pk_f16_f32 v23, v48, v49
	v_pk_max_f16 v22, v22, 0
	v_pk_max_f16 v23, v23, 0
	ds_write2_b64 v30, v[26:27], v[22:23] offset0:16 offset1:24
	s_waitcnt lgkmcnt(1)
	v_mfma_f32_32x32x16_f16 v[2:17], v[50:53], v[18:21], v[2:17]
	v_mad_u32_u24 v18, v28, s7, v107
	v_lshl_or_b32 v42, s66, 5, v116
	s_cselect_b32 s8, 0xf60, 0
	s_movk_i32 s9, 0xff0
	s_cselect_b32 s9, s9, 0x80
	s_cselect_b32 s15, s15, 0x110
	s_cselect_b32 s16, s16, 0x190
	s_nop 4
	v_cvt_pk_f16_f32 v2, v2, v3
	v_cvt_pk_f16_f32 v3, v4, v5
	v_cvt_pk_f16_f32 v4, v6, v7
	v_cvt_pk_f16_f32 v5, v8, v9
	v_pk_max_f16 v2, v2, 0
	v_pk_max_f16 v3, v3, 0
	v_pk_max_f16 v4, v4, 0
	v_pk_max_f16 v5, v5, 0
	ds_write2_b64 v18, v[2:3], v[4:5] offset1:8
	v_cvt_pk_f16_f32 v2, v10, v11
	v_cvt_pk_f16_f32 v3, v12, v13
	v_cvt_pk_f16_f32 v4, v14, v15
	v_cvt_pk_f16_f32 v5, v16, v17
	v_pk_max_f16 v2, v2, 0
	v_pk_max_f16 v3, v3, 0
	v_pk_max_f16 v4, v4, 0
	v_pk_max_f16 v5, v5, 0
	ds_write2_b64 v18, v[2:3], v[4:5] offset0:16 offset1:24
	v_mul_lo_u16_e32 v2, 24, v114
	v_lshrrev_b16_e32 v2, 7, v2
	v_and_b32_e32 v2, 6, v2
	v_add_u32_sdwa v103, v114, v2 dst_sel:DWORD dst_unused:UNUSED_PAD src0_sel:DWORD src1_sel:WORD_0
	v_mul_lo_u16_e32 v2, 47, v99
	v_mov_b32_e32 v3, 14
	v_and_b32_sdwa v6, v2, v3 dst_sel:DWORD dst_unused:UNUSED_PAD src0_sel:BYTE_1 src1_sel:DWORD
	v_add_u32_e32 v106, v99, v6
	s_waitcnt vmcnt(0)
	v_mad_u32_u24 v90, v103, s7, v42
	v_mad_u32_u24 v91, v106, s7, v42
	v_add_u32_e32 v2, s8, v90
	v_add_u32_e32 v6, s8, v91
	s_waitcnt lgkmcnt(0)
	s_barrier
	ds_read_b128 v[2:5], v2
	ds_read_b128 v[6:9], v6
	s_waitcnt lgkmcnt(1)
	v_mfma_f32_32x32x16_f16 v[18:33], v[82:85], v[2:5], 0
	v_add_u32_e32 v34, s9, v90
	v_add_u32_e32 v38, s9, v91
	ds_read_b128 v[34:37], v34
	ds_read_b128 v[38:41], v38
	s_cselect_b32 s17, s17, 0x220
	v_or_b32_e32 v101, 0x60, v114
	s_waitcnt lgkmcnt(2)
	v_mfma_f32_32x32x16_f16 v[2:17], v[82:85], v[6:9], 0
	s_waitcnt lgkmcnt(1)
	v_mfma_f32_32x32x16_f16 v[18:33], v[74:77], v[34:37], v[18:33]
	v_add_u32_e32 v34, s15, v90
	ds_read_b128 v[34:37], v34
	s_waitcnt lgkmcnt(1)
	v_mfma_f32_32x32x16_f16 v[2:17], v[74:77], v[38:41], v[2:17]
	v_add_u32_e32 v38, s15, v91
	ds_read_b128 v[38:41], v38
	s_waitcnt lgkmcnt(1)
	v_mfma_f32_32x32x16_f16 v[18:33], v[78:81], v[34:37], v[18:33]
	v_add_u32_e32 v34, s16, v90
	ds_read_b128 v[34:37], v34
	s_waitcnt lgkmcnt(1)
	v_mfma_f32_32x32x16_f16 v[2:17], v[78:81], v[38:41], v[2:17]
	v_add_u32_e32 v38, s16, v91
	ds_read_b128 v[38:41], v38
	s_waitcnt lgkmcnt(1)
	v_mfma_f32_32x32x16_f16 v[18:33], v[70:73], v[34:37], v[18:33]
	v_mul_lo_u16_e32 v34, 0xbb, v102
	v_lshrrev_b16_e32 v34, 10, v34
	v_and_b32_e32 v43, 30, v34
	v_add_u32_e32 v34, s17, v90
	ds_read_b128 v[34:37], v34
	v_add_u32_e32 v104, v102, v43
	v_mad_u32_u24 v92, v104, s7, v42
	s_waitcnt lgkmcnt(1)
	v_mfma_f32_32x32x16_f16 v[2:17], v[70:73], v[38:41], v[2:17]
	v_add_u32_e32 v38, s17, v91
	ds_read_b128 v[38:41], v38
	s_waitcnt lgkmcnt(1)
	v_mfma_f32_32x32x16_f16 v[18:33], v[66:69], v[34:37], v[18:33]
	v_min_u32_e32 v34, 0x78, v101
	v_mul_lo_u16_e32 v35, 0xbb, v34
	v_lshrrev_b16_e32 v35, 10, v35
	v_and_b32_e32 v35, 30, v35
	v_add_u32_e32 v105, v34, v35
	v_mad_u32_u24 v93, v105, s7, v42
	s_waitcnt lgkmcnt(0)
	v_mfma_f32_32x32x16_f16 v[2:17], v[66:69], v[38:41], v[2:17]
	v_add_u32_e32 v34, s8, v92
	v_add_u32_e32 v38, s8, v93
	ds_read_b128 v[34:37], v34
	ds_read_b128 v[38:41], v38
	v_add_u32_e32 v86, s9, v93
	s_waitcnt lgkmcnt(1)
	v_mfma_f32_32x32x16_f16 v[50:65], v[82:85], v[34:37], 0
	ds_read_b128 v[86:89], v86
	s_waitcnt lgkmcnt(1)
	v_mfma_f32_32x32x16_f16 v[34:49], v[82:85], v[38:41], 0
	v_add_u32_e32 v82, s9, v92
	ds_read_b128 v[82:85], v82
	s_waitcnt lgkmcnt(0)
	v_mfma_f32_32x32x16_f16 v[50:65], v[74:77], v[82:85], v[50:65]
	v_add_u32_e32 v82, s15, v93
	ds_read_b128 v[82:85], v82
	v_mfma_f32_32x32x16_f16 v[34:49], v[74:77], v[86:89], v[34:49]
	v_add_u32_e32 v74, s15, v92
	ds_read_b128 v[74:77], v74
	s_waitcnt lgkmcnt(0)
	v_mfma_f32_32x32x16_f16 v[50:65], v[78:81], v[74:77], v[50:65]
	v_add_u32_e32 v74, s16, v92
	ds_read_b128 v[74:77], v74
	v_mfma_f32_32x32x16_f16 v[34:49], v[78:81], v[82:85], v[34:49]
	v_add_u32_e32 v78, s16, v93
	ds_read_b128 v[78:81], v78
	s_waitcnt lgkmcnt(1)
	v_mfma_f32_32x32x16_f16 v[50:65], v[70:73], v[74:77], v[50:65]
	v_add_u32_e32 v74, s17, v93
	ds_read_b128 v[74:77], v74
	s_waitcnt lgkmcnt(1)
	v_mfma_f32_32x32x16_f16 v[34:49], v[70:73], v[78:81], v[34:49]
	v_add_u32_e32 v70, s17, v92
	ds_read_b128 v[70:73], v70
	s_waitcnt lgkmcnt(0)
	v_mfma_f32_32x32x16_f16 v[50:65], v[66:69], v[70:73], v[50:65]
	v_mfma_f32_32x32x16_f16 v[34:49], v[66:69], v[74:77], v[34:49]
	s_movk_i32 s7, 0x1cb0
	s_cselect_b32 s7, s7, 0x2a0
	v_add_u32_e32 v74, s7, v90
	ds_read_b128 v[74:77], v74
	v_add_u32_e32 v78, s7, v91
	ds_read_b128 v[78:81], v78
	s_movk_i32 s12, 0x1d30
	s_cselect_b32 s12, s12, 0xdd0
	s_movk_i32 s8, 0x1dc0
	s_cselect_b32 s8, s8, 0xe50
	s_movk_i32 s9, 0x1e40
	s_cselect_b32 s9, s9, 0xee0
	s_waitcnt vmcnt(0) lgkmcnt(1)
	v_mfma_f32_32x32x16_f16 v[18:33], v[108:111], v[74:77], v[18:33]
	v_add_u32_e32 v82, s12, v91
	ds_read_b128 v[82:85], v82
	s_waitcnt lgkmcnt(1)
	v_mfma_f32_32x32x16_f16 v[2:17], v[108:111], v[78:81], v[2:17]
	v_add_u32_e32 v78, s12, v90
	ds_read_b128 v[78:81], v78
	s_waitcnt lgkmcnt(0)
	v_mfma_f32_32x32x16_f16 v[18:33], v[118:121], v[78:81], v[18:33]
	v_add_u32_e32 v86, s8, v91
	ds_read_b128 v[86:89], v86
	v_mfma_f32_32x32x16_f16 v[2:17], v[118:121], v[82:85], v[2:17]
	v_add_u32_e32 v82, s8, v90
	ds_read_b128 v[82:85], v82
	s_waitcnt lgkmcnt(0)
	v_mfma_f32_32x32x16_f16 v[18:33], v[122:125], v[82:85], v[18:33]
	v_add_u32_e32 v82, s9, v90
	ds_read_b128 v[82:85], v82
	v_mfma_f32_32x32x16_f16 v[2:17], v[122:125], v[86:89], v[2:17]
	v_add_u32_e32 v86, s9, v91
	ds_read_b128 v[86:89], v86
	s_waitcnt lgkmcnt(1)
	v_mfma_f32_32x32x16_f16 v[18:33], v[94:97], v[82:85], v[18:33]
	s_waitcnt lgkmcnt(0)
	v_mfma_f32_32x32x16_f16 v[2:17], v[94:97], v[86:89], v[2:17]
	v_add_u32_e32 v82, s7, v92
	v_add_u32_e32 v86, s7, v93
	ds_read_b128 v[82:85], v82
	ds_read_b128 v[86:89], v86
	s_waitcnt lgkmcnt(1)
	v_mfma_f32_32x32x16_f16 v[50:65], v[108:111], v[82:85], v[50:65]
	v_add_u32_e32 v82, s12, v93
	ds_read_b128 v[82:85], v82
	s_waitcnt lgkmcnt(1)
	v_mfma_f32_32x32x16_f16 v[34:49], v[108:111], v[86:89], v[34:49]
	v_add_u32_e32 v66, s12, v92
	ds_read_b128 v[66:69], v66
	s_waitcnt lgkmcnt(0)
	v_mfma_f32_32x32x16_f16 v[50:65], v[118:121], v[66:69], v[50:65]
	v_add_u32_e32 v66, s8, v92
	ds_read_b128 v[66:69], v66
	v_mfma_f32_32x32x16_f16 v[34:49], v[118:121], v[82:85], v[34:49]
	v_add_u32_e32 v70, s8, v93
	ds_read_b128 v[70:73], v70
	s_waitcnt lgkmcnt(1)
	v_mfma_f32_32x32x16_f16 v[50:65], v[122:125], v[66:69], v[50:65]
	v_add_u32_e32 v66, s9, v92
	ds_read_b128 v[66:69], v66
	s_waitcnt lgkmcnt(1)
	v_mfma_f32_32x32x16_f16 v[34:49], v[122:125], v[70:73], v[34:49]
	v_add_u32_e32 v70, s9, v93
	ds_read_b128 v[70:73], v70
	s_waitcnt lgkmcnt(1)
	v_mfma_f32_32x32x16_f16 v[50:65], v[94:97], v[66:69], v[50:65]
	s_waitcnt lgkmcnt(0)
	v_mfma_f32_32x32x16_f16 v[34:49], v[94:97], v[70:73], v[34:49]
	s_cmpk_gt_u32 s3, 0x17f
	s_barrier
	s_cbranch_scc1 .LBB1_17
	s_mul_hi_u32 s7, s42, 0x55555556
	s_mul_i32 s7, s7, 3
	s_sub_i32 s7, s42, s7
	s_lshl_b32 s7, s7, 3
	s_add_i32 s8, s7, 0xb600
	s_cmpk_gt_u32 s3, 0xbf
	v_mad_u32_u24 v109, v115, 24, s7
	s_cselect_b32 s7, 0x60, 0
	v_or_b32_e32 v112, s7, v114
	v_mul_lo_u16_e32 v66, 0x4f, v112
	v_lshrrev_b16_e32 v66, 9, v66
	v_and_b32_e32 v66, 30, v66
	v_add_u32_e32 v66, v112, v66
	v_mov_b32_e32 v111, s8
	v_mul_u32_u24_e32 v110, 0x48, v115
	v_add_u32_e32 v107, 0xf550, v98
	v_mad_u32_u24 v113, v66, s6, v111
	ds_read_b128 v[76:79], v107 offset:5120
	v_add_u32_e32 v117, v113, v110
	ds_read2_b64 v[118:121], v117 offset0:4 offset1:5
	ds_read_b128 v[122:125], v98 offset:62800
	v_mul_u32_u24_e32 v108, 0x438, v115
	v_add_u32_e32 v113, v113, v108
	s_waitcnt lgkmcnt(2)
	v_mov_b32_e32 v66, v76
	v_mov_b32_e32 v67, v76
	v_mov_b32_e32 v68, v76
	v_mov_b32_e32 v69, v76
	v_mov_b32_e32 v70, v77
	v_mov_b32_e32 v71, v77
	v_mov_b32_e32 v72, v77
	v_mov_b32_e32 v73, v77
	v_mov_b32_e32 v74, v78
	v_mov_b32_e32 v75, v78
	v_mov_b32_e32 v76, v78
	v_mov_b32_e32 v77, v78
	v_mov_b32_e32 v78, v79
	v_mov_b32_e32 v80, v79
	v_mov_b32_e32 v81, v79
	s_movk_i32 s8, 0xd0
	v_mad_u32_u24 v112, v112, s8, v109
	s_waitcnt lgkmcnt(0)
	v_mfma_f32_32x32x16_f16 v[82:97], v[122:125], v[118:121], v[66:81]
	ds_read2_b64 v[118:121], v117 offset0:139 offset1:140
	ds_read_b128 v[122:125], v98 offset:63824
	s_waitcnt lgkmcnt(0)
	v_mfma_f32_32x32x16_f16 v[82:97], v[122:125], v[118:121], v[82:97]
	v_add_u32_e32 v118, 0x8d8, v117
	ds_read2_b64 v[118:121], v118 offset1:1
	ds_read_b128 v[122:125], v98 offset:64848
	s_waitcnt lgkmcnt(0)
	v_mfma_f32_32x32x16_f16 v[82:97], v[122:125], v[118:121], v[82:97]
	ds_read2_b64 v[118:121], v113 offset0:22 offset1:23
	ds_read_b128 v[122:125], v107 offset:3072
	v_add_u32_e32 v113, 0x890, v117
	s_waitcnt lgkmcnt(0)
	v_mfma_f32_32x32x16_f16 v[82:97], v[122:125], v[118:121], v[82:97]
	ds_read2_b64 v[118:121], v113 offset1:1
	ds_read_b128 v[122:125], v107 offset:4096
	s_waitcnt lgkmcnt(0)
	v_mfma_f32_32x32x16_f16 v[82:97], v[122:125], v[118:121], v[82:97]
	s_nop 11
	v_cvt_pk_f16_f32 v82, v82, v83
	v_cvt_pk_f16_f32 v83, v84, v85
	v_cvt_pk_f16_f32 v84, v86, v87
	v_cvt_pk_f16_f32 v85, v88, v89
	v_pk_max_f16 v82, v82, 0
	v_pk_max_f16 v83, v83, 0
	v_pk_max_f16 v84, v84, 0
	v_pk_max_f16 v85, v85, 0
	ds_write2_b64 v112, v[82:83], v[84:85] offset1:6
	v_cvt_pk_f16_f32 v82, v90, v91
	v_cvt_pk_f16_f32 v83, v92, v93
	v_cvt_pk_f16_f32 v84, v94, v95
	v_cvt_pk_f16_f32 v85, v96, v97
	v_pk_max_f16 v82, v82, 0
	v_pk_max_f16 v83, v83, 0
	v_pk_max_f16 v84, v84, 0
	v_pk_max_f16 v85, v85, 0
	ds_write2_b64 v112, v[82:83], v[84:85] offset0:12 offset1:18
	s_add_i32 s9, s7, 32
	v_or_b32_e32 v112, s9, v114
	v_mul_lo_u16_e32 v82, 0x4f, v112
	v_lshrrev_b16_e32 v82, 9, v82
	v_and_b32_e32 v82, 62, v82
	v_add_u32_e32 v82, v112, v82
	v_mad_u32_u24 v113, v82, s6, v111
	v_add_u32_e32 v117, v113, v110
	ds_read2_b64 v[118:121], v117 offset0:4 offset1:5
	ds_read_b128 v[122:125], v98 offset:62800
	v_add_u32_e32 v113, v113, v108
	v_mad_u32_u24 v112, v112, s8, v109
	s_waitcnt lgkmcnt(0)
	v_mfma_f32_32x32x16_f16 v[82:97], v[122:125], v[118:121], v[66:81]
	ds_read2_b64 v[118:121], v117 offset0:139 offset1:140
	ds_read_b128 v[122:125], v98 offset:63824
	s_waitcnt lgkmcnt(0)
	v_mfma_f32_32x32x16_f16 v[82:97], v[122:125], v[118:121], v[82:97]
	v_add_u32_e32 v118, 0x8d8, v117
	ds_read2_b64 v[118:121], v118 offset1:1
	ds_read_b128 v[122:125], v98 offset:64848
	s_waitcnt lgkmcnt(0)
	v_mfma_f32_32x32x16_f16 v[82:97], v[122:125], v[118:121], v[82:97]
	ds_read2_b64 v[118:121], v113 offset0:22 offset1:23
	ds_read_b128 v[122:125], v107 offset:3072
	v_add_u32_e32 v113, 0x890, v117
	s_waitcnt lgkmcnt(0)
	v_mfma_f32_32x32x16_f16 v[82:97], v[122:125], v[118:121], v[82:97]
	ds_read2_b64 v[118:121], v113 offset1:1
	ds_read_b128 v[122:125], v107 offset:4096
	s_waitcnt lgkmcnt(0)
	v_mfma_f32_32x32x16_f16 v[82:97], v[122:125], v[118:121], v[82:97]
	s_nop 11
	v_cvt_pk_f16_f32 v82, v82, v83
	v_cvt_pk_f16_f32 v83, v84, v85
	v_cvt_pk_f16_f32 v84, v86, v87
	v_cvt_pk_f16_f32 v85, v88, v89
	v_pk_max_f16 v82, v82, 0
	v_pk_max_f16 v83, v83, 0
	v_pk_max_f16 v84, v84, 0
	v_pk_max_f16 v85, v85, 0
	ds_write2_b64 v112, v[82:83], v[84:85] offset1:6
	v_cvt_pk_f16_f32 v82, v90, v91
	v_cvt_pk_f16_f32 v83, v92, v93
	v_cvt_pk_f16_f32 v84, v94, v95
	v_cvt_pk_f16_f32 v85, v96, v97
	v_pk_max_f16 v82, v82, 0
	v_pk_max_f16 v83, v83, 0
	v_pk_max_f16 v84, v84, 0
	v_pk_max_f16 v85, v85, 0
	ds_write2_b64 v112, v[82:83], v[84:85] offset0:12 offset1:18
	s_add_i32 s7, s7, 64
	v_or_b32_e32 v82, s7, v114
	v_min_u32_e32 v112, 0xa8, v82
	v_mul_lo_u16_e32 v82, 0x4f, v112
	v_lshrrev_b16_e32 v82, 9, v82
	v_and_b32_e32 v86, 62, v82
	ds_read_b128 v[82:85], v98 offset:62800
	v_add_u32_e32 v86, v112, v86
	v_mad_u32_u24 v111, v86, s6, v111
	v_add_u32_e32 v110, v111, v110
	ds_read2_b64 v[86:89], v110 offset0:4 offset1:5
	ds_read2_b64 v[90:93], v110 offset0:139 offset1:140
	v_add_u32_e32 v94, 0x890, v110
	ds_read2_b64 v[94:97], v94 offset1:1
	s_waitcnt lgkmcnt(2)
	v_mfma_f32_32x32x16_f16 v[66:81], v[82:85], v[86:89], v[66:81]
	ds_read_b128 v[82:85], v98 offset:63824
	ds_read_b128 v[86:89], v98 offset:64848
	s_waitcnt lgkmcnt(1)
	v_mfma_f32_32x32x16_f16 v[66:81], v[82:85], v[90:93], v[66:81]
	v_add_u32_e32 v82, 0x8d8, v110
	ds_read2_b64 v[82:85], v82 offset1:1
	v_add_u32_e32 v90, v111, v108
	ds_read2_b64 v[90:93], v90 offset0:22 offset1:23
	s_waitcnt lgkmcnt(1)
	v_mfma_f32_32x32x16_f16 v[66:81], v[86:89], v[82:85], v[66:81]
	ds_read_b128 v[82:85], v107 offset:3072
	ds_read_b128 v[86:89], v107 offset:4096
	s_waitcnt lgkmcnt(1)
	v_mfma_f32_32x32x16_f16 v[66:81], v[82:85], v[90:93], v[66:81]
	v_mad_u32_u24 v82, v112, s8, v109
	s_waitcnt lgkmcnt(0)
	v_mfma_f32_32x32x16_f16 v[66:81], v[86:89], v[94:97], v[66:81]
	s_nop 11
	v_cvt_pk_f16_f32 v66, v66, v67
	v_cvt_pk_f16_f32 v67, v68, v69
	v_cvt_pk_f16_f32 v68, v70, v71
	v_cvt_pk_f16_f32 v69, v72, v73
	v_cvt_pk_f16_f32 v70, v74, v75
	v_cvt_pk_f16_f32 v71, v76, v77
	v_cvt_pk_f16_f32 v72, v78, v79
	v_cvt_pk_f16_f32 v73, v80, v81
	v_pk_max_f16 v66, v66, 0
	v_pk_max_f16 v67, v67, 0
	v_pk_max_f16 v68, v68, 0
	v_pk_max_f16 v69, v69, 0
	v_pk_max_f16 v70, v70, 0
	v_pk_max_f16 v71, v71, 0
	v_pk_max_f16 v72, v72, 0
	v_pk_max_f16 v73, v73, 0
	ds_write2_b64 v82, v[66:67], v[68:69] offset1:6
	ds_write2_b64 v82, v[70:71], v[72:73] offset0:12 offset1:18

.LBB1_46:
	v_lshlrev_b32_e32 v39, 2, v0
	s_mov_b64 exec, 0x1fffff
	global_load_dword v40, v39, s[24:25]
	global_load_dword v41, v39, s[52:53]
	global_load_dword v44, v39, s[58:59]
	global_load_dword v12, v39, s[30:31]
	global_load_dword v13, v39, s[10:11]
	global_load_dword v27, v39, s[42:43]
	global_load_dword v28, v39, s[12:13]
	global_load_dword v29, v39, s[54:55]
	global_load_dword v30, v39, s[56:57]
	global_load_dword v31, v39, s[60:61]
	s_mov_b64 exec, 0xff
	global_load_dword v36, v39, s[16:17]
	s_mov_b64 exec, -1
	global_load_dword v37, v39, s[14:15]
	global_load_dword v38, v39, s[18:19]
	v_add_u32_e32 v1, 0xf550, v98
	ds_write_b128 v98, v[86:89] offset:62800
	ds_write_b128 v98, v[62:65] offset:63824
	ds_write_b128 v98, v[58:61] offset:64848
	ds_write_b128 v1, v[54:57] offset:3072
	ds_write_b128 v1, v[50:53] offset:4096
	ds_write_b128 v1, v[46:49] offset:5120
	v_cmp_gt_u32_e64 s[4:5], 21, v0
	v_lshlrev_b32_e32 v1, 2, v0
	s_and_saveexec_b64 s[64:65], s[4:5]
	s_cbranch_execz .LBB1_6
